# baseline (speedup 1.0000x reference)
.LBB0_40:
	s_waitcnt lgkmcnt(0)
	ds_read_b64_tr_b16 v[124:125], v215 offset:0
	ds_read_b64_tr_b16 v[126:127], v215 offset:0x800
	ds_read_b64_tr_b16 v[120:121], v215 offset:0x200
	ds_read_b64_tr_b16 v[122:123], v215 offset:0xa00
	ds_read_b64_tr_b16 v[116:117], v215 offset:0x400
	ds_read_b64_tr_b16 v[118:119], v215 offset:0xc00
	ds_read_b64_tr_b16 v[112:113], v215 offset:0x600
	ds_read_b64_tr_b16 v[114:115], v215 offset:0xe00
	ds_read_b64_tr_b16 v[108:109], v215 offset:0x1000
	ds_read_b64_tr_b16 v[110:111], v215 offset:0x1800
	ds_read_b64_tr_b16 v[104:105], v215 offset:0x1200
	ds_read_b64_tr_b16 v[106:107], v215 offset:0x1a00
	ds_read_b64_tr_b16 v[100:101], v215 offset:0x1400
	ds_read_b64_tr_b16 v[102:103], v215 offset:0x1c00
	v_exp_f32_e32 v159, v40
	v_cvt_pk_bf16_f32 v40, v64, v65
	v_exp_f32_e32 v160, v41
	v_cvt_pk_bf16_f32 v41, v66, v67
	v_exp_f32_e32 v161, v42
	v_exp_f32_e32 v162, v43
	v_cvt_pk_bf16_f32 v42, v68, v69
	v_cvt_pk_bf16_f32 v43, v70, v71
	s_waitcnt lgkmcnt(12)
	s_nop 1
	v_mfma_f32_32x32x16_bf16 a[0:15], v[124:127], v[40:43], a[0:15]
	ds_read_b64_tr_b16 v[96:97], v215 offset:0x1600
	ds_read_b64_tr_b16 v[98:99], v215 offset:0x1e00
	v_exp_f32_e32 v141, v56
	v_exp_f32_e32 v142, v57
	v_exp_f32_e32 v143, v58
	v_exp_f32_e32 v144, v59
	v_cvt_pk_bf16_f32 v56, v80, v81
	v_cvt_pk_bf16_f32 v57, v82, v83
	v_cvt_pk_bf16_f32 v58, v84, v85
	v_cvt_pk_bf16_f32 v59, v86, v87
	s_nop 1
	v_mfma_f32_32x32x16_bf16 a[16:31], v[124:127], v[56:59], a[16:31]
	v_exp_f32_e32 v149, v32
	v_exp_f32_e32 v150, v33
	v_exp_f32_e32 v151, v34
	s_waitcnt lgkmcnt(12)
	v_mfma_f32_32x32x16_bf16 a[32:47], v[120:123], v[40:43], a[32:47]
	ds_read_b64_tr_b16 v[28:29], v215 offset:0x2000
	ds_read_b64_tr_b16 v[30:31], v215 offset:0x2800
	v_exp_f32_e32 v154, v35
	v_cvt_pk_bf16_f32 v32, v72, v73
	v_cvt_pk_bf16_f32 v33, v74, v75
	v_cvt_pk_bf16_f32 v34, v76, v77
	v_cvt_pk_bf16_f32 v35, v78, v79
	v_mfma_f32_32x32x16_bf16 a[48:63], v[120:123], v[56:59], a[48:63]
	v_exp_f32_e32 v131, v48
	v_exp_f32_e32 v134, v49
	v_exp_f32_e32 v135, v50
	s_waitcnt lgkmcnt(12)
	v_mfma_f32_32x32x16_bf16 a[64:79], v[116:119], v[40:43], a[64:79]
	ds_read_b64_tr_b16 v[24:25], v215 offset:0x2200
	ds_read_b64_tr_b16 v[26:27], v215 offset:0x2a00
	v_exp_f32_e32 v136, v51
	v_cvt_pk_bf16_f32 v48, v88, v89
	v_cvt_pk_bf16_f32 v49, v90, v91
	v_cvt_pk_bf16_f32 v50, v92, v93
	v_cvt_pk_bf16_f32 v51, v94, v95
	v_mfma_f32_32x32x16_bf16 a[80:95], v[116:119], v[56:59], a[80:95]
	v_exp_f32_e32 v137, v52
	v_exp_f32_e32 v138, v53
	v_exp_f32_e32 v139, v54
	s_waitcnt lgkmcnt(12)
	v_mfma_f32_32x32x16_bf16 a[96:111], v[112:115], v[40:43], a[96:111]
	ds_read_b64_tr_b16 v[20:21], v215 offset:0x2400
	ds_read_b64_tr_b16 v[22:23], v215 offset:0x2c00
	v_exp_f32_e32 v140, v55
	v_exp_f32_e32 v163, v44
	v_exp_f32_e32 v164, v45
	v_mfma_f32_32x32x16_bf16 a[112:127], v[112:115], v[56:59], a[112:127]
	v_exp_f32_e32 v165, v46
	v_exp_f32_e32 v166, v47
	v_cvt_pk_bf16_f32 v44, v131, v134
	v_cvt_pk_bf16_f32 v45, v135, v136
	s_waitcnt lgkmcnt(12)
	v_mfma_f32_32x32x16_bf16 a[0:15], v[108:111], v[32:35], a[0:15]
	ds_read_b64_tr_b16 v[16:17], v215 offset:0x2600
	ds_read_b64_tr_b16 v[18:19], v215 offset:0x2e00
	v_cvt_pk_bf16_f32 v46, v137, v138
	v_cvt_pk_bf16_f32 v47, v139, v140
	v_exp_f32_e32 v155, v36
	v_exp_f32_e32 v145, v60
	v_mfma_f32_32x32x16_bf16 a[16:31], v[108:111], v[48:51], a[16:31]
	v_exp_f32_e32 v146, v61
	v_exp_f32_e32 v156, v37
	v_exp_f32_e32 v157, v38
	s_waitcnt lgkmcnt(12)
	v_mfma_f32_32x32x16_bf16 a[32:47], v[104:107], v[32:35], a[32:47]
	ds_read_b64_tr_b16 v[12:13], v215 offset:0x3000
	ds_read_b64_tr_b16 v[14:15], v215 offset:0x3800
	v_exp_f32_e32 v147, v62
	v_exp_f32_e32 v148, v63
	v_exp_f32_e32 v158, v39
	v_mfma_f32_32x32x16_bf16 a[48:63], v[104:107], v[48:51], a[48:63]
	v_cvt_pk_bf16_f32 v60, v149, v150
	v_cvt_pk_bf16_f32 v61, v151, v154
	v_cvt_pk_bf16_f32 v62, v155, v156
	v_cvt_pk_bf16_f32 v63, v157, v158
	v_cvt_pk_bf16_f32 v36, v141, v142
	v_cvt_pk_bf16_f32 v37, v143, v144
	s_waitcnt lgkmcnt(12)
	v_mfma_f32_32x32x16_bf16 a[64:79], v[100:103], v[32:35], a[64:79]
	ds_read_b64_tr_b16 v[8:9], v215 offset:0x3200
	ds_read_b64_tr_b16 v[10:11], v215 offset:0x3a00
	v_cvt_pk_bf16_f32 v38, v145, v146
	v_cvt_pk_bf16_f32 v39, v147, v148
	v_cvt_pk_bf16_f32 v52, v159, v160
	v_cvt_pk_bf16_f32 v53, v161, v162
	v_cvt_pk_bf16_f32 v54, v163, v164
	v_cvt_pk_bf16_f32 v55, v165, v166
	v_mfma_f32_32x32x16_bf16 a[80:95], v[100:103], v[48:51], a[80:95]
	v_lshrrev_b32_e32 v128, 5, v204
	v_add_f32_e32 v64, v133, v131
	v_add_f32_e32 v65, v132, v134
	v_add_f32_e32 v64, v64, v135
	v_add_f32_e32 v65, v65, v136
	v_add_f32_e32 v64, v64, v137
	s_waitcnt lgkmcnt(12)
	v_mfma_f32_32x32x16_bf16 a[96:111], v[96:99], v[32:35], a[96:111]
	ds_read_b64_tr_b16 v[4:5], v215 offset:0x3400
	ds_read_b64_tr_b16 v[6:7], v215 offset:0x3c00
	v_add_f32_e32 v65, v65, v138
	v_add_f32_e32 v64, v64, v139
	v_add_f32_e32 v65, v65, v140
	v_add_f32_e32 v66, v129, v149
	v_add_f32_e32 v64, v64, v141
	v_add_f32_e32 v65, v65, v142
	v_mfma_f32_32x32x16_bf16 a[112:127], v[96:99], v[48:51], a[112:127]
	v_add_f32_e32 v67, v130, v150
	v_add_f32_e32 v66, v66, v151
	v_add_f32_e32 v64, v64, v143
	v_add_f32_e32 v65, v65, v144
	v_add_f32_e32 v67, v67, v154
	v_add_f32_e32 v66, v66, v155
	s_waitcnt lgkmcnt(12)
	v_mfma_f32_32x32x16_bf16 a[0:15], v[28:31], v[44:47], a[0:15]
	ds_read_b64_tr_b16 v[0:1], v215 offset:0x3600
	ds_read_b64_tr_b16 v[2:3], v215 offset:0x3e00
	v_add_f32_e32 v64, v64, v145
	v_add_f32_e32 v65, v65, v146
	v_add_f32_e32 v67, v67, v156
	v_add_f32_e32 v66, v66, v157
	v_add_f32_e32 v64, v64, v147
	v_add_f32_e32 v65, v65, v148
	v_mfma_f32_32x32x16_bf16 a[16:31], v[28:31], v[60:63], a[16:31]
	v_add_f32_e32 v67, v67, v158
	v_add_f32_e32 v66, v66, v159
	v_add_f32_e32 v67, v67, v160
	v_add_f32_e32 v66, v66, v161
	v_add_f32_e32 v64, v64, v65
	v_mov_b32_e32 v65, v64
	s_waitcnt lgkmcnt(12)
	v_mfma_f32_32x32x16_bf16 a[32:47], v[24:27], v[44:47], a[32:47]
	v_add_f32_e32 v67, v67, v162
	v_add_f32_e32 v66, v66, v163
	v_permlane32_swap_b32_e32 v64, v65
	v_add_f32_e32 v67, v67, v164
	v_add_f32_e32 v66, v66, v165
	v_add_f32_e32 v64, v64, v65
	v_mfma_f32_32x32x16_bf16 a[48:63], v[24:27], v[60:63], a[48:63]
	v_add_f32_e32 v67, v67, v166
	v_add_f32_e32 v65, v153, v64
	v_add_f32_e32 v64, v66, v67
	v_mov_b32_e32 v66, v64
	s_nop 1
	v_permlane32_swap_b32_e32 v64, v66
	v_add_f32_e32 v64, v64, v66
	s_waitcnt lgkmcnt(10)
	v_mfma_f32_32x32x16_bf16 a[64:79], v[20:23], v[44:47], a[64:79]
	v_add_f32_e32 v64, v152, v64
	v_cmp_lt_f32_e32 vcc, 0, v65
	v_readfirstlane_b32 s0, v200
	s_and_b32 s9, s9, 0xffff
	s_mov_b32 s11, 0x20000
	s_mov_b32 s10, 0x1000000
	s_nop 1
	s_lshl_b32 s0, s0, 8
	v_xor_b32_e32 v43, v208, v204
	v_mfma_f32_32x32x16_bf16 a[80:95], v[20:23], v[60:63], a[80:95]
	v_lshlrev_b32_e32 v43, 5, v43
	v_xor_b32_e32 v59, v210, v204
	v_lshlrev_b32_e32 v42, 9, v208
	v_and_b32_e32 v43, 0x1e0, v43
	v_lshlrev_b32_e32 v59, 5, v59
	v_add3_u32 v87, v201, v42, v43
	s_waitcnt lgkmcnt(8)
	v_mfma_f32_32x32x16_bf16 a[96:111], v[16:19], v[44:47], a[96:111]
	v_lshlrev_b32_e32 v58, 9, v210
	v_lshlrev_b32_e32 v35, 9, v207
	v_xor_b32_e32 v51, v209, v204
	v_lshlrev_b32_e32 v51, 5, v51
	v_lshlrev_b32_e32 v50, 9, v209
	v_and_b32_e32 v51, 0x1e0, v51
	v_mfma_f32_32x32x16_bf16 a[112:127], v[16:19], v[60:63], a[112:127]
	v_xor_b32_e32 v27, v206, v204
	v_lshlrev_b32_e32 v27, 5, v27
	v_lshlrev_b32_e32 v26, 9, v206
	v_and_b32_e32 v27, 0x1e0, v27
	v_add3_u32 v85, v201, v26, v27
	v_and_b32_e32 v59, 0x1e0, v59
	s_waitcnt lgkmcnt(6)
	v_mfma_f32_32x32x16_bf16 a[0:15], v[12:15], v[36:39], a[0:15]
	v_add3_u32 v88, v201, v50, v51
	v_add3_u32 v89, v201, v58, v59
	s_or_b32 s1, s0, 0x400
	v_mfma_f32_32x32x16_bf16 a[16:31], v[12:15], v[52:55], a[16:31]
	s_waitcnt lgkmcnt(4)
	v_mfma_f32_32x32x16_bf16 a[32:47], v[8:11], v[36:39], a[32:47]
	v_mfma_f32_32x32x16_bf16 a[48:63], v[8:11], v[52:55], a[48:63]
	s_waitcnt lgkmcnt(2)
	v_mfma_f32_32x32x16_bf16 a[64:79], v[4:7], v[36:39], a[64:79]
	v_mfma_f32_32x32x16_bf16 a[80:95], v[4:7], v[52:55], a[80:95]
	v_lshlrev_b32_e32 v6, 1, v204
	v_bitop3_b32 v20, v128, v6, 30 bitop3:0x78
	s_waitcnt lgkmcnt(0)
	v_mfma_f32_32x32x16_bf16 a[96:111], v[0:3], v[36:39], a[96:111]
	v_mfma_f32_32x32x16_bf16 a[112:127], v[0:3], v[52:55], a[112:127]
	s_waitcnt lgkmcnt(0)
	v_rcp_f32_e32 v2, v65
	v_lshlrev_b32_e32 v0, 9, v204
	v_and_b32_e32 v0, 0x3e00, v0
	v_add_u32_e32 v1, v201, v0
	v_cndmask_b32_e32 v7, 0, v2, vcc
	v_accvgpr_read_b32 v2, a0
	v_accvgpr_read_b32 v3, a1
	v_accvgpr_read_b32 v4, a2
	v_accvgpr_read_b32 v5, a3
	v_accvgpr_read_b32 v8, a4
	v_accvgpr_read_b32 v9, a5
	v_accvgpr_read_b32 v10, a6
	v_accvgpr_read_b32 v11, a7
	v_accvgpr_read_b32 v12, a8
	v_accvgpr_read_b32 v13, a9
	v_accvgpr_read_b32 v14, a10
	v_accvgpr_read_b32 v15, a11
	v_accvgpr_read_b32 v16, a12
	v_accvgpr_read_b32 v17, a13
	v_accvgpr_read_b32 v18, a14
	v_accvgpr_read_b32 v19, a15

	v_lshl_add_u32 v62, v20, 4, v1
	v_mul_f32_e32 v2, v2, v7
	v_mul_f32_e32 v3, v3, v7
	v_mul_f32_e32 v4, v4, v7
	v_mul_f32_e32 v5, v5, v7
	ds_write_b128 v62, v[2:5]
	v_mul_f32_e32 v2, v8, v7
	v_add_u32_e32 v8, 2, v128
	v_bitop3_b32 v8, v8, v6, 30 bitop3:0x78
	v_lshl_add_u32 v63, v8, 4, v1
	v_add_u32_e32 v8, 4, v128
	v_bitop3_b32 v8, v8, v6, 30 bitop3:0x78
	v_mul_f32_e32 v3, v9, v7
	v_mul_f32_e32 v4, v10, v7
	v_mul_f32_e32 v5, v11, v7
	v_lshl_add_u32 v65, v8, 4, v1
	v_add_u32_e32 v8, 6, v128
	ds_write_b128 v63, v[2:5]
	v_mul_f32_e32 v2, v12, v7
	v_mul_f32_e32 v3, v13, v7
	v_mul_f32_e32 v4, v14, v7
	v_mul_f32_e32 v5, v15, v7
	v_bitop3_b32 v8, v8, v6, 30 bitop3:0x78
	ds_write_b128 v65, v[2:5]
	v_mul_f32_e32 v2, v16, v7
	v_mul_f32_e32 v3, v17, v7
	v_mul_f32_e32 v4, v18, v7
	v_mul_f32_e32 v5, v19, v7
	v_lshl_add_u32 v70, v8, 4, v1
	v_add_u32_e32 v20, 8, v128
	ds_write_b128 v70, v[2:5]
	v_accvgpr_read_b32 v2, a32
	v_accvgpr_read_b32 v3, a33
	v_accvgpr_read_b32 v4, a34
	v_accvgpr_read_b32 v5, a35
	v_accvgpr_read_b32 v8, a36
	v_accvgpr_read_b32 v9, a37
	v_accvgpr_read_b32 v10, a38
	v_accvgpr_read_b32 v11, a39
	v_accvgpr_read_b32 v12, a40
	v_accvgpr_read_b32 v13, a41
	v_accvgpr_read_b32 v14, a42
	v_accvgpr_read_b32 v15, a43
	v_accvgpr_read_b32 v16, a44
	v_accvgpr_read_b32 v17, a45
	v_accvgpr_read_b32 v18, a46
	v_accvgpr_read_b32 v19, a47

	v_bitop3_b32 v20, v20, v6, 30 bitop3:0x78
	v_mul_f32_e32 v2, v2, v7
	v_lshl_add_u32 v71, v20, 4, v1
	v_mul_f32_e32 v3, v3, v7
	v_mul_f32_e32 v4, v4, v7
	v_mul_f32_e32 v5, v5, v7
	ds_write_b128 v71, v[2:5]
	v_mul_f32_e32 v2, v8, v7
	v_add_u32_e32 v8, 10, v128
	v_bitop3_b32 v8, v8, v6, 30 bitop3:0x78
	v_lshl_add_u32 v72, v8, 4, v1
	v_add_u32_e32 v8, 12, v128
	v_bitop3_b32 v8, v8, v6, 30 bitop3:0x78
	v_mul_f32_e32 v3, v9, v7
	v_mul_f32_e32 v4, v10, v7
	v_mul_f32_e32 v5, v11, v7
	v_lshl_add_u32 v73, v8, 4, v1
	v_add_u32_e32 v8, 14, v128
	ds_write_b128 v72, v[2:5]
	v_mul_f32_e32 v2, v12, v7
	v_mul_f32_e32 v3, v13, v7
	v_mul_f32_e32 v4, v14, v7
	v_mul_f32_e32 v5, v15, v7
	v_bitop3_b32 v8, v8, v6, 30 bitop3:0x78
	ds_write_b128 v73, v[2:5]
	v_mul_f32_e32 v2, v16, v7
	v_mul_f32_e32 v3, v17, v7
	v_mul_f32_e32 v4, v18, v7
	v_mul_f32_e32 v5, v19, v7
	v_lshl_add_u32 v74, v8, 4, v1
	v_add_u32_e32 v20, 16, v128
	ds_write_b128 v74, v[2:5]
	v_accvgpr_read_b32 v2, a64
	v_accvgpr_read_b32 v3, a65
	v_accvgpr_read_b32 v4, a66
	v_accvgpr_read_b32 v5, a67
	v_accvgpr_read_b32 v8, a68
	v_accvgpr_read_b32 v9, a69
	v_accvgpr_read_b32 v10, a70
	v_accvgpr_read_b32 v11, a71
	v_accvgpr_read_b32 v12, a72
	v_accvgpr_read_b32 v13, a73
	v_accvgpr_read_b32 v14, a74
	v_accvgpr_read_b32 v15, a75
	v_accvgpr_read_b32 v16, a76
	v_accvgpr_read_b32 v17, a77
	v_accvgpr_read_b32 v18, a78
	v_accvgpr_read_b32 v19, a79

	v_bitop3_b32 v20, v20, v6, 30 bitop3:0x78
	v_mul_f32_e32 v2, v2, v7
	v_lshl_add_u32 v75, v20, 4, v1
	v_mul_f32_e32 v3, v3, v7
	v_mul_f32_e32 v4, v4, v7
	v_mul_f32_e32 v5, v5, v7
	ds_write_b128 v75, v[2:5]
	v_mul_f32_e32 v2, v8, v7
	v_add_u32_e32 v8, 18, v128
	v_bitop3_b32 v8, v8, v6, 30 bitop3:0x78
	v_lshl_add_u32 v76, v8, 4, v1
	v_add_u32_e32 v8, 20, v128
	v_bitop3_b32 v8, v8, v6, 30 bitop3:0x78
	v_mul_f32_e32 v3, v9, v7
	v_mul_f32_e32 v4, v10, v7
	v_mul_f32_e32 v5, v11, v7
	v_lshl_add_u32 v77, v8, 4, v1
	v_add_u32_e32 v8, 22, v128
	ds_write_b128 v76, v[2:5]
	v_mul_f32_e32 v2, v12, v7
	v_mul_f32_e32 v3, v13, v7
	v_mul_f32_e32 v4, v14, v7
	v_mul_f32_e32 v5, v15, v7
	v_bitop3_b32 v8, v8, v6, 30 bitop3:0x78
	ds_write_b128 v77, v[2:5]
	v_mul_f32_e32 v2, v16, v7
	v_mul_f32_e32 v3, v17, v7
	v_mul_f32_e32 v4, v18, v7
	v_mul_f32_e32 v5, v19, v7
	v_lshl_add_u32 v78, v8, 4, v1
	v_add_u32_e32 v20, 24, v128
	ds_write_b128 v78, v[2:5]
	v_accvgpr_read_b32 v2, a96
	v_accvgpr_read_b32 v3, a97
	v_accvgpr_read_b32 v4, a98
	v_accvgpr_read_b32 v5, a99
	v_accvgpr_read_b32 v8, a100
	v_accvgpr_read_b32 v9, a101
	v_accvgpr_read_b32 v10, a102
	v_accvgpr_read_b32 v11, a103
	v_accvgpr_read_b32 v12, a104
	v_accvgpr_read_b32 v13, a105
	v_accvgpr_read_b32 v14, a106
	v_accvgpr_read_b32 v15, a107
	v_accvgpr_read_b32 v16, a108
	v_accvgpr_read_b32 v17, a109
	v_accvgpr_read_b32 v18, a110
	v_accvgpr_read_b32 v19, a111

	v_bitop3_b32 v20, v20, v6, 30 bitop3:0x78
	v_mul_f32_e32 v2, v2, v7
	v_lshl_add_u32 v79, v20, 4, v1
	v_mul_f32_e32 v3, v3, v7
	v_mul_f32_e32 v4, v4, v7
	v_mul_f32_e32 v5, v5, v7
	ds_write_b128 v79, v[2:5]
	v_mul_f32_e32 v2, v8, v7
	v_add_u32_e32 v8, 26, v128
	v_bitop3_b32 v8, v8, v6, 30 bitop3:0x78
	v_lshl_add_u32 v80, v8, 4, v1
	v_add_u32_e32 v8, 28, v128
	v_mul_f32_e32 v3, v9, v7
	v_mul_f32_e32 v4, v10, v7
	v_mul_f32_e32 v5, v11, v7
	v_bitop3_b32 v8, v8, v6, 30 bitop3:0x78
	ds_write_b128 v80, v[2:5]
	v_mul_f32_e32 v2, v12, v7
	v_mul_f32_e32 v3, v13, v7
	v_mul_f32_e32 v4, v14, v7
	v_mul_f32_e32 v5, v15, v7
	v_lshl_add_u32 v81, v8, 4, v1
	ds_write_b128 v81, v[2:5]
	v_mul_f32_e32 v2, v16, v7
	v_mul_f32_e32 v3, v17, v7
	v_mul_f32_e32 v4, v18, v7
	v_mul_f32_e32 v5, v19, v7
	v_add_u32_e32 v7, 30, v128
	v_bitop3_b32 v6, v7, v6, 30 bitop3:0x78
	v_lshl_add_u32 v1, v6, 4, v1
	ds_write_b128 v1, v[2:5]
	v_xor_b32_e32 v3, v202, v204
	v_lshlrev_b32_e32 v3, 5, v3
	v_xor_b32_e32 v11, v203, v204
	v_lshlrev_b32_e32 v2, 9, v202
	v_and_b32_e32 v34, 0x1e0, v3
	v_lshlrev_b32_e32 v11, 5, v11
	v_xor_b32_e32 v19, v205, v204
	s_waitcnt lgkmcnt(0)
	v_add3_u32 v82, v201, v2, v34
	v_lshlrev_b32_e32 v10, 9, v203
	v_and_b32_e32 v11, 0x1e0, v11
	v_lshlrev_b32_e32 v19, 5, v19
	ds_read_b128 v[2:5], v82
	ds_read_b128 v[6:9], v82 offset:16
	v_add3_u32 v83, v201, v10, v11
	v_lshlrev_b32_e32 v18, 9, v205
	v_and_b32_e32 v19, 0x1e0, v19
	ds_read_b128 v[10:13], v83
	ds_read_b128 v[14:17], v83 offset:16
	v_add3_u32 v84, v201, v18, v19
	ds_read_b128 v[18:21], v84
	ds_read_b128 v[22:25], v84 offset:16
	ds_read_b128 v[26:29], v85
	ds_read_b128 v[30:33], v85 offset:16
	v_add3_u32 v86, v201, v35, v34
	ds_read_b128 v[34:37], v86
	ds_read_b128 v[38:41], v86 offset:16
	v_lshlrev_b32_e32 v0, 4, v204
	ds_read_b128 v[42:45], v87
	ds_read_b128 v[46:49], v87 offset:16
	s_waitcnt lgkmcnt(11)
	v_cvt_pk_bf16_f32 v2, v2, v3
	v_cvt_pk_bf16_f32 v3, v4, v5
	s_waitcnt lgkmcnt(10)
	v_cvt_pk_bf16_f32 v4, v6, v7
	v_cvt_pk_bf16_f32 v5, v8, v9
	ds_read_b128 v[50:53], v88
	ds_read_b128 v[54:57], v88 offset:16
	ds_read_b128 v[58:61], v89
	ds_read_b128 v[66:69], v89 offset:16
	buffer_store_dwordx4 v[2:5], v0, s[8:11], s0 offen sc1
	s_waitcnt lgkmcnt(13)
	v_cvt_pk_bf16_f32 v2, v10, v11
	v_cvt_pk_bf16_f32 v3, v12, v13
	s_waitcnt lgkmcnt(12)
	v_cvt_pk_bf16_f32 v4, v14, v15
	v_cvt_pk_bf16_f32 v5, v16, v17
	buffer_store_dwordx4 v[2:5], v0, s[8:11], s1 offen sc1
	s_or_b32 s1, s0, 0x800
	s_waitcnt lgkmcnt(11)
	v_cvt_pk_bf16_f32 v2, v18, v19
	v_cvt_pk_bf16_f32 v3, v20, v21
	s_waitcnt lgkmcnt(10)
	v_cvt_pk_bf16_f32 v4, v22, v23
	v_cvt_pk_bf16_f32 v5, v24, v25
	buffer_store_dwordx4 v[2:5], v0, s[8:11], s1 offen sc1
	s_or_b32 s1, s0, 0xc00
	s_waitcnt lgkmcnt(9)
	v_cvt_pk_bf16_f32 v2, v26, v27
	v_cvt_pk_bf16_f32 v3, v28, v29
	s_waitcnt lgkmcnt(8)
	v_cvt_pk_bf16_f32 v4, v30, v31
	v_cvt_pk_bf16_f32 v5, v32, v33
	buffer_store_dwordx4 v[2:5], v0, s[8:11], s1 offen sc1
	s_or_b32 s1, s0, 0x1000
	s_waitcnt lgkmcnt(7)
	v_cvt_pk_bf16_f32 v2, v34, v35
	v_cvt_pk_bf16_f32 v3, v36, v37
	s_waitcnt lgkmcnt(6)
	v_cvt_pk_bf16_f32 v4, v38, v39
	v_cvt_pk_bf16_f32 v5, v40, v41
	buffer_store_dwordx4 v[2:5], v0, s[8:11], s1 offen sc1
	s_or_b32 s1, s0, 0x1400
	s_waitcnt lgkmcnt(5)
	v_cvt_pk_bf16_f32 v2, v42, v43
	v_cvt_pk_bf16_f32 v3, v44, v45
	s_waitcnt lgkmcnt(4)
	v_cvt_pk_bf16_f32 v4, v46, v47
	v_cvt_pk_bf16_f32 v5, v48, v49
	buffer_store_dwordx4 v[2:5], v0, s[8:11], s1 offen sc1
	s_or_b32 s1, s0, 0x1800
	s_waitcnt lgkmcnt(3)
	v_cvt_pk_bf16_f32 v2, v50, v51
	v_cvt_pk_bf16_f32 v3, v52, v53
	s_waitcnt lgkmcnt(2)
	v_cvt_pk_bf16_f32 v4, v54, v55
	v_cvt_pk_bf16_f32 v5, v56, v57
	v_rcp_f32_e32 v6, v64
	buffer_store_dwordx4 v[2:5], v0, s[8:11], s1 offen sc1
	s_or_b32 s1, s0, 0x1c00
	s_waitcnt lgkmcnt(1)
	v_cvt_pk_bf16_f32 v2, v58, v59
	v_cvt_pk_bf16_f32 v3, v60, v61
	s_waitcnt lgkmcnt(0)
	v_cvt_pk_bf16_f32 v4, v66, v67
	v_cvt_pk_bf16_f32 v5, v68, v69
	buffer_store_dwordx4 v[2:5], v0, s[8:11], s1 offen sc1
	s_waitcnt lgkmcnt(0)
	v_cmp_lt_f32_e32 vcc, 0, v64
	v_accvgpr_read_b32 v2, a16
	v_accvgpr_read_b32 v3, a17
	v_accvgpr_read_b32 v4, a18
	v_accvgpr_read_b32 v5, a19
	v_accvgpr_read_b32 v7, a20
	v_accvgpr_read_b32 v8, a21
	v_accvgpr_read_b32 v9, a22
	v_accvgpr_read_b32 v10, a23
	v_accvgpr_read_b32 v11, a24
	v_accvgpr_read_b32 v12, a25
	v_accvgpr_read_b32 v13, a26
	v_accvgpr_read_b32 v14, a27
	v_accvgpr_read_b32 v15, a28
	v_accvgpr_read_b32 v16, a29
	v_accvgpr_read_b32 v17, a30
	v_accvgpr_read_b32 v18, a31

	s_or_b32 s1, s0, 0x2000
	v_cndmask_b32_e32 v6, 0, v6, vcc
	v_mul_f32_e32 v2, v2, v6
	v_mul_f32_e32 v3, v3, v6
	v_mul_f32_e32 v4, v4, v6
	v_mul_f32_e32 v5, v5, v6
	ds_write_b128 v62, v[2:5]
	v_mul_f32_e32 v2, v7, v6
	v_mul_f32_e32 v3, v8, v6
	v_mul_f32_e32 v4, v9, v6
	v_mul_f32_e32 v5, v10, v6
	ds_write_b128 v63, v[2:5]
	v_mul_f32_e32 v2, v11, v6
	v_mul_f32_e32 v3, v12, v6
	v_mul_f32_e32 v4, v13, v6
	v_mul_f32_e32 v5, v14, v6
	ds_write_b128 v65, v[2:5]
	v_mul_f32_e32 v2, v15, v6
	v_mul_f32_e32 v3, v16, v6
	v_mul_f32_e32 v4, v17, v6
	v_mul_f32_e32 v5, v18, v6
	ds_write_b128 v70, v[2:5]
	v_accvgpr_read_b32 v2, a48
	v_accvgpr_read_b32 v3, a49
	v_accvgpr_read_b32 v4, a50
	v_accvgpr_read_b32 v5, a51
	v_accvgpr_read_b32 v7, a52
	v_accvgpr_read_b32 v8, a53
	v_accvgpr_read_b32 v9, a54
	v_accvgpr_read_b32 v10, a55
	v_accvgpr_read_b32 v11, a56
	v_accvgpr_read_b32 v12, a57
	v_accvgpr_read_b32 v13, a58
	v_accvgpr_read_b32 v14, a59
	v_accvgpr_read_b32 v15, a60
	v_accvgpr_read_b32 v16, a61
	v_accvgpr_read_b32 v17, a62
	v_accvgpr_read_b32 v18, a63

	v_mul_f32_e32 v2, v2, v6
	v_mul_f32_e32 v3, v3, v6
	v_mul_f32_e32 v4, v4, v6
	v_mul_f32_e32 v5, v5, v6
	ds_write_b128 v71, v[2:5]
	v_mul_f32_e32 v2, v7, v6
	v_mul_f32_e32 v3, v8, v6
	v_mul_f32_e32 v4, v9, v6
	v_mul_f32_e32 v5, v10, v6
	ds_write_b128 v72, v[2:5]
	v_mul_f32_e32 v2, v11, v6
	v_mul_f32_e32 v3, v12, v6
	v_mul_f32_e32 v4, v13, v6
	v_mul_f32_e32 v5, v14, v6
	ds_write_b128 v73, v[2:5]
	v_mul_f32_e32 v2, v15, v6
	v_mul_f32_e32 v3, v16, v6
	v_mul_f32_e32 v4, v17, v6
	v_mul_f32_e32 v5, v18, v6
	ds_write_b128 v74, v[2:5]
	v_accvgpr_read_b32 v2, a80
	v_accvgpr_read_b32 v3, a81
	v_accvgpr_read_b32 v4, a82
	v_accvgpr_read_b32 v5, a83
	v_accvgpr_read_b32 v7, a84
	v_accvgpr_read_b32 v8, a85
	v_accvgpr_read_b32 v9, a86
	v_accvgpr_read_b32 v10, a87
	v_accvgpr_read_b32 v11, a88
	v_accvgpr_read_b32 v12, a89
	v_accvgpr_read_b32 v13, a90
	v_accvgpr_read_b32 v14, a91
	v_accvgpr_read_b32 v15, a92
	v_accvgpr_read_b32 v16, a93
	v_accvgpr_read_b32 v17, a94
	v_accvgpr_read_b32 v18, a95

	v_mul_f32_e32 v2, v2, v6
	v_mul_f32_e32 v3, v3, v6
	v_mul_f32_e32 v4, v4, v6
	v_mul_f32_e32 v5, v5, v6
	ds_write_b128 v75, v[2:5]
	v_mul_f32_e32 v2, v7, v6
	v_mul_f32_e32 v3, v8, v6
	v_mul_f32_e32 v4, v9, v6
	v_mul_f32_e32 v5, v10, v6
	ds_write_b128 v76, v[2:5]
	v_mul_f32_e32 v2, v11, v6
	v_mul_f32_e32 v3, v12, v6
	v_mul_f32_e32 v4, v13, v6
	v_mul_f32_e32 v5, v14, v6
	ds_write_b128 v77, v[2:5]
	v_mul_f32_e32 v2, v15, v6
	v_mul_f32_e32 v3, v16, v6
	v_mul_f32_e32 v4, v17, v6
	v_mul_f32_e32 v5, v18, v6
	ds_write_b128 v78, v[2:5]
	v_accvgpr_read_b32 v2, a112
	v_accvgpr_read_b32 v3, a113
	v_accvgpr_read_b32 v4, a114
	v_accvgpr_read_b32 v5, a115
	v_accvgpr_read_b32 v7, a116
	v_accvgpr_read_b32 v8, a117
	v_accvgpr_read_b32 v9, a118
	v_accvgpr_read_b32 v10, a119
	v_accvgpr_read_b32 v11, a120
	v_accvgpr_read_b32 v12, a121
	v_accvgpr_read_b32 v13, a122
	v_accvgpr_read_b32 v14, a123
	v_accvgpr_read_b32 v15, a124
	v_accvgpr_read_b32 v16, a125
	v_accvgpr_read_b32 v17, a126
	v_accvgpr_read_b32 v18, a127

	v_mul_f32_e32 v2, v2, v6
	v_mul_f32_e32 v3, v3, v6
	v_mul_f32_e32 v4, v4, v6
	v_mul_f32_e32 v5, v5, v6
	ds_write_b128 v79, v[2:5]
	v_mul_f32_e32 v2, v7, v6
	v_mul_f32_e32 v3, v8, v6
	v_mul_f32_e32 v4, v9, v6
	v_mul_f32_e32 v5, v10, v6
	ds_write_b128 v80, v[2:5]
	v_mul_f32_e32 v2, v11, v6
	v_mul_f32_e32 v3, v12, v6
	v_mul_f32_e32 v4, v13, v6
	v_mul_f32_e32 v5, v14, v6
	ds_write_b128 v81, v[2:5]
	v_mul_f32_e32 v2, v15, v6
	v_mul_f32_e32 v3, v16, v6
	v_mul_f32_e32 v4, v17, v6
	v_mul_f32_e32 v5, v18, v6
	ds_write_b128 v1, v[2:5]
	s_waitcnt lgkmcnt(0)
	ds_read_b128 v[2:5], v82
	ds_read_b128 v[6:9], v82 offset:16
	ds_read_b128 v[10:13], v83
	ds_read_b128 v[14:17], v83 offset:16
	ds_read_b128 v[18:21], v84
	ds_read_b128 v[22:25], v84 offset:16
	ds_read_b128 v[26:29], v85
	ds_read_b128 v[30:33], v85 offset:16
	ds_read_b128 v[34:37], v86
	ds_read_b128 v[38:41], v86 offset:16
	ds_read_b128 v[42:45], v87
	ds_read_b128 v[46:49], v87 offset:16
	ds_read_b128 v[50:53], v88
	ds_read_b128 v[54:57], v88 offset:16
	ds_read_b128 v[58:61], v89
	ds_read_b128 v[62:65], v89 offset:16
	s_waitcnt lgkmcnt(14)
	v_cvt_pk_bf16_f32 v2, v2, v3
	v_cvt_pk_bf16_f32 v3, v4, v5
	v_cvt_pk_bf16_f32 v4, v6, v7
	v_cvt_pk_bf16_f32 v5, v8, v9
	buffer_store_dwordx4 v[2:5], v0, s[8:11], s1 offen sc1
	s_or_b32 s1, s0, 0x2400
	s_waitcnt lgkmcnt(13)
	v_cvt_pk_bf16_f32 v2, v10, v11
	v_cvt_pk_bf16_f32 v3, v12, v13
	s_waitcnt lgkmcnt(12)
	v_cvt_pk_bf16_f32 v4, v14, v15
	v_cvt_pk_bf16_f32 v5, v16, v17
	buffer_store_dwordx4 v[2:5], v0, s[8:11], s1 offen sc1
	s_or_b32 s1, s0, 0x2800
	s_waitcnt lgkmcnt(11)
	v_cvt_pk_bf16_f32 v2, v18, v19
	v_cvt_pk_bf16_f32 v3, v20, v21
	s_waitcnt lgkmcnt(10)
	v_cvt_pk_bf16_f32 v4, v22, v23
	v_cvt_pk_bf16_f32 v5, v24, v25
	buffer_store_dwordx4 v[2:5], v0, s[8:11], s1 offen sc1
	s_or_b32 s1, s0, 0x2c00
	s_waitcnt lgkmcnt(9)
	v_cvt_pk_bf16_f32 v2, v26, v27
	v_cvt_pk_bf16_f32 v3, v28, v29
	s_waitcnt lgkmcnt(8)
	v_cvt_pk_bf16_f32 v4, v30, v31
	v_cvt_pk_bf16_f32 v5, v32, v33
	buffer_store_dwordx4 v[2:5], v0, s[8:11], s1 offen sc1
	s_or_b32 s1, s0, 0x3000
	s_waitcnt lgkmcnt(7)
	v_cvt_pk_bf16_f32 v2, v34, v35
	v_cvt_pk_bf16_f32 v3, v36, v37
	s_waitcnt lgkmcnt(6)
	v_cvt_pk_bf16_f32 v4, v38, v39
	v_cvt_pk_bf16_f32 v5, v40, v41
	buffer_store_dwordx4 v[2:5], v0, s[8:11], s1 offen sc1
	s_or_b32 s1, s0, 0x3400
	s_waitcnt lgkmcnt(5)
	v_cvt_pk_bf16_f32 v2, v42, v43
	v_cvt_pk_bf16_f32 v3, v44, v45
	s_waitcnt lgkmcnt(4)
	v_cvt_pk_bf16_f32 v4, v46, v47
	v_cvt_pk_bf16_f32 v5, v48, v49
	buffer_store_dwordx4 v[2:5], v0, s[8:11], s1 offen sc1
	s_or_b32 s1, s0, 0x3800
	s_waitcnt lgkmcnt(3)
	v_cvt_pk_bf16_f32 v2, v50, v51
	v_cvt_pk_bf16_f32 v3, v52, v53
	s_waitcnt lgkmcnt(2)
	v_cvt_pk_bf16_f32 v4, v54, v55
	v_cvt_pk_bf16_f32 v5, v56, v57
	buffer_store_dwordx4 v[2:5], v0, s[8:11], s1 offen sc1
	s_or_b32 s0, s0, 0x3c00
	s_waitcnt lgkmcnt(1)
	v_cvt_pk_bf16_f32 v2, v58, v59
	v_cvt_pk_bf16_f32 v3, v60, v61
	s_waitcnt lgkmcnt(0)
	v_cvt_pk_bf16_f32 v4, v62, v63
	v_cvt_pk_bf16_f32 v5, v64, v65
	buffer_store_dwordx4 v[2:5], v0, s[8:11], s0 offen sc1
	s_waitcnt lgkmcnt(0)
	s_endpgm
